# layer2 self rows also loaded late (in set-B tail) instead of in the prologue
# speedup vs baseline: 1.3164x; 1.0087x over previous
.Lg2_active:
	s_mov_b32 s60, 0x00ff00ff
	s_mov_b32 s61, 0x0c030c01
	v_lshrrev_b32_e32 v107, 3, v1
	v_and_b32_e32 v108, 7, v1
	v_and_b32_e32 v105, 15, v1
	v_lshrrev_b32_e32 v106, 4, v1
	s_bfe_u32 s36, s3, 0x10002
	s_lshl_b32 s58, s36, 3
	s_xor_b32 s59, s58, 8
	v_or_b32_e32 v102, s58, v107
	v_or_b32_e32 v103, s59, v107
	v_lshlrev_b32_e32 v89, 4, v108
	v_and_b32_e32 v90, 56, v1
	v_lshlrev_b32_e32 v90, 2, v90
	s_waitcnt lgkmcnt(0)
	s_lshl_b32 s58, s6, 8
	s_add_u32 s32, s16, s58
	s_addc_u32 s33, s17, 0
	s_lshl_b32 s58, s6, 10
	s_add_u32 s34, s18, s58
	s_addc_u32 s35, s19, 0
	v_lshlrev_b32_e32 v109, 4, v105
	global_load_dword v104, v109, s[32:33] offset:8
	v_lshlrev_b32_e32 v110, 4, v102
	global_load_dwordx2 v[68:69], v110, s[32:33]
	v_lshlrev_b32_e32 v111, 4, v103
	global_load_dwordx2 v[70:71], v111, s[32:33]
	v_lshlrev_b32_e32 v101, 2, v108
	v_lshl_or_b32 v110, v102, 6, v101
	global_load_dword v60, v110, s[34:35]
	global_load_dword v61, v110, s[34:35] offset:32
	v_lshl_or_b32 v111, v103, 6, v101
	global_load_dword v62, v111, s[34:35]
	global_load_dword v63, v111, s[34:35] offset:32
	global_load_dwordx4 v[2:5], v95, s[22:23]
	global_load_dwordx4 v[6:9], v98, s[22:23]
	global_load_dwordx4 v[10:13], v99, s[22:23]
	global_load_dwordx4 v[14:17], v100, s[22:23]
	v_and_b32_e32 v101, 0x7f, v0
	v_lshlrev_b32_e32 v101, 2, v101
	global_load_dword v19, v101, s[24:25]
	s_mul_i32 s48, s3, 0x1100
	s_add_u32 s48, s48, 0x10200
	v_mul_u32_u24_e32 v91, 0x110, v102
	v_lshl_add_u32 v91, v108, 5, v91
	v_add_u32_e32 v91, s48, v91
	v_mul_u32_u24_e32 v92, 0x110, v103
	v_lshl_add_u32 v92, v108, 5, v92
	v_add_u32_e32 v92, s48, v92
	s_waitcnt vmcnt(5)
	v_readlane_b32 s49, v69, 0
	v_readlane_b32 s50, v69, 8
	v_readlane_b32 s51, v69, 16
	v_readlane_b32 s52, v69, 24
	v_readlane_b32 s53, v69, 32
	v_readlane_b32 s54, v69, 40
	v_readlane_b32 s55, v69, 48
	v_readlane_b32 s56, v69, 56
	s_max_i32 s37, s49, s50
	s_max_i32 s37, s37, s51
	s_max_i32 s37, s37, s52
	s_max_i32 s37, s37, s53
	s_max_i32 s37, s37, s54
	s_max_i32 s37, s37, s55
	s_max_i32 s37, s37, s56
	v_readlane_b32 s49, v71, 0
	v_readlane_b32 s50, v71, 8
	v_readlane_b32 s51, v71, 16
	v_readlane_b32 s52, v71, 24
	v_readlane_b32 s53, v71, 32
	v_readlane_b32 s54, v71, 40
	v_readlane_b32 s55, v71, 48
	v_readlane_b32 s56, v71, 56
	s_max_i32 s38, s49, s50
	s_max_i32 s38, s38, s51
	s_max_i32 s38, s38, s52
	s_max_i32 s38, s38, s53
	s_max_i32 s38, s38, s54
	s_max_i32 s38, s38, s55
	s_max_i32 s38, s38, s56
	v_and_b32_e32 v103, 0xffff, v60
	v_lshlrev_b32_e32 v103, 1, v103
	global_load_ushort v52, v103, s[14:15]
	v_lshrrev_b32_e32 v109, 16, v60
	v_lshlrev_b32_e32 v109, 1, v109
	global_load_ushort v53, v109, s[14:15]
	v_and_b32_e32 v103, 0xffff, v61
	v_lshlrev_b32_e32 v103, 1, v103
	global_load_ushort v54, v103, s[14:15]
	v_lshrrev_b32_e32 v109, 16, v61
	v_lshlrev_b32_e32 v109, 1, v109
	global_load_ushort v55, v109, s[14:15]
	v_and_b32_e32 v103, 0xffff, v62
	v_lshlrev_b32_e32 v103, 1, v103
	global_load_ushort v56, v103, s[14:15]
	v_lshrrev_b32_e32 v109, 16, v62
	v_lshlrev_b32_e32 v109, 1, v109
	global_load_ushort v57, v109, s[14:15]
	v_and_b32_e32 v103, 0xffff, v63
	v_lshlrev_b32_e32 v103, 1, v103
	global_load_ushort v58, v103, s[14:15]
	v_lshrrev_b32_e32 v109, 16, v63
	v_lshlrev_b32_e32 v109, 1, v109
	global_load_ushort v59, v109, s[14:15]
	v_lshlrev_b32_e32 v103, 8, v104
	v_lshl_or_b32 v103, v106, 4, v103
	s_waitcnt vmcnt(8)
	ds_write_b128 v96, v[2:5]
	ds_write_b128 v96, v[6:9] offset:16384
	ds_write_b128 v96, v[10:13] offset:32768
	ds_write_b128 v96, v[14:17] offset:49152
	v_add_u32_e32 v101, 0x10000, v101
	ds_write_b32 v101, v19
	s_waitcnt lgkmcnt(0)
	s_barrier
	s_mov_b32 s39, 0
	s_waitcnt vmcnt(0)
	v_lshl_or_b32 v64, v53, 16, v52
	v_lshl_or_b32 v65, v55, 16, v54
	v_lshl_or_b32 v66, v57, 16, v56
	v_lshl_or_b32 v67, v59, 16, v58

.Lg2_tail0:
	s_cmp_eq_u32 s39, 1
	s_cbranch_scc1 .Lg2_tailb0
	s_waitcnt vmcnt(7)
	v_cvt_f32_ubyte0_e32 v85, v20
	v_cvt_f32_ubyte1_e32 v86, v20
	v_cvt_f32_ubyte2_e32 v87, v20
	v_cvt_f32_ubyte3_e32 v88, v20
	v_fmac_f32_e32 v2, v85, v52
	v_fmac_f32_e32 v3, v86, v52
	v_fmac_f32_e32 v4, v87, v52
	v_fmac_f32_e32 v5, v88, v52
	v_cvt_f32_ubyte0_e32 v85, v21
	v_cvt_f32_ubyte1_e32 v86, v21
	v_cvt_f32_ubyte2_e32 v87, v21
	v_cvt_f32_ubyte3_e32 v88, v21
	v_fmac_f32_e32 v6, v85, v52
	v_fmac_f32_e32 v7, v86, v52
	v_fmac_f32_e32 v8, v87, v52
	v_fmac_f32_e32 v9, v88, v52
	v_cvt_f32_ubyte0_e32 v85, v22
	v_cvt_f32_ubyte1_e32 v86, v22
	v_cvt_f32_ubyte2_e32 v87, v22
	v_cvt_f32_ubyte3_e32 v88, v22
	v_fmac_f32_e32 v10, v85, v52
	v_fmac_f32_e32 v11, v86, v52
	v_fmac_f32_e32 v12, v87, v52
	v_fmac_f32_e32 v13, v88, v52
	v_cvt_f32_ubyte0_e32 v85, v23
	v_cvt_f32_ubyte1_e32 v86, v23
	v_cvt_f32_ubyte2_e32 v87, v23
	v_cvt_f32_ubyte3_e32 v88, v23
	v_fmac_f32_e32 v14, v85, v52
	v_fmac_f32_e32 v15, v86, v52
	v_fmac_f32_e32 v16, v87, v52
	v_fmac_f32_e32 v17, v88, v52
	s_waitcnt vmcnt(6)
	v_cvt_f32_ubyte0_e32 v85, v24
	v_cvt_f32_ubyte1_e32 v86, v24
	v_cvt_f32_ubyte2_e32 v87, v24
	v_cvt_f32_ubyte3_e32 v88, v24
	v_fmac_f32_e32 v2, v85, v53
	v_fmac_f32_e32 v3, v86, v53
	v_fmac_f32_e32 v4, v87, v53
	v_fmac_f32_e32 v5, v88, v53
	v_cvt_f32_ubyte0_e32 v85, v25
	v_cvt_f32_ubyte1_e32 v86, v25
	v_cvt_f32_ubyte2_e32 v87, v25
	v_cvt_f32_ubyte3_e32 v88, v25
	v_fmac_f32_e32 v6, v85, v53
	v_fmac_f32_e32 v7, v86, v53
	v_fmac_f32_e32 v8, v87, v53
	v_fmac_f32_e32 v9, v88, v53
	v_cvt_f32_ubyte0_e32 v85, v26
	v_cvt_f32_ubyte1_e32 v86, v26
	v_cvt_f32_ubyte2_e32 v87, v26
	v_cvt_f32_ubyte3_e32 v88, v26
	v_fmac_f32_e32 v10, v85, v53
	v_fmac_f32_e32 v11, v86, v53
	v_fmac_f32_e32 v12, v87, v53
	v_fmac_f32_e32 v13, v88, v53
	v_cvt_f32_ubyte0_e32 v85, v27
	v_cvt_f32_ubyte1_e32 v86, v27
	v_cvt_f32_ubyte2_e32 v87, v27
	v_cvt_f32_ubyte3_e32 v88, v27
	v_fmac_f32_e32 v14, v85, v53
	v_fmac_f32_e32 v15, v86, v53
	v_fmac_f32_e32 v16, v87, v53
	v_fmac_f32_e32 v17, v88, v53
	s_waitcnt vmcnt(5)
	v_cvt_f32_ubyte0_e32 v85, v28
	v_cvt_f32_ubyte1_e32 v86, v28
	v_cvt_f32_ubyte2_e32 v87, v28
	v_cvt_f32_ubyte3_e32 v88, v28
	v_fmac_f32_e32 v2, v85, v54
	v_fmac_f32_e32 v3, v86, v54
	v_fmac_f32_e32 v4, v87, v54
	v_fmac_f32_e32 v5, v88, v54
	v_cvt_f32_ubyte0_e32 v85, v29
	v_cvt_f32_ubyte1_e32 v86, v29
	v_cvt_f32_ubyte2_e32 v87, v29
	v_cvt_f32_ubyte3_e32 v88, v29
	v_fmac_f32_e32 v6, v85, v54
	v_fmac_f32_e32 v7, v86, v54
	v_fmac_f32_e32 v8, v87, v54
	v_fmac_f32_e32 v9, v88, v54
	v_cvt_f32_ubyte0_e32 v85, v30
	v_cvt_f32_ubyte1_e32 v86, v30
	v_cvt_f32_ubyte2_e32 v87, v30
	v_cvt_f32_ubyte3_e32 v88, v30
	v_fmac_f32_e32 v10, v85, v54
	v_fmac_f32_e32 v11, v86, v54
	v_fmac_f32_e32 v12, v87, v54
	v_fmac_f32_e32 v13, v88, v54
	v_cvt_f32_ubyte0_e32 v85, v31
	v_cvt_f32_ubyte1_e32 v86, v31
	v_cvt_f32_ubyte2_e32 v87, v31
	v_cvt_f32_ubyte3_e32 v88, v31
	v_fmac_f32_e32 v14, v85, v54
	v_fmac_f32_e32 v15, v86, v54
	v_fmac_f32_e32 v16, v87, v54
	v_fmac_f32_e32 v17, v88, v54
	s_waitcnt vmcnt(4)
	v_cvt_f32_ubyte0_e32 v85, v32
	v_cvt_f32_ubyte1_e32 v86, v32
	v_cvt_f32_ubyte2_e32 v87, v32
	v_cvt_f32_ubyte3_e32 v88, v32
	v_fmac_f32_e32 v2, v85, v55
	v_fmac_f32_e32 v3, v86, v55
	v_fmac_f32_e32 v4, v87, v55
	v_fmac_f32_e32 v5, v88, v55
	v_cvt_f32_ubyte0_e32 v85, v33
	v_cvt_f32_ubyte1_e32 v86, v33
	v_cvt_f32_ubyte2_e32 v87, v33
	v_cvt_f32_ubyte3_e32 v88, v33
	v_fmac_f32_e32 v6, v85, v55
	v_fmac_f32_e32 v7, v86, v55
	v_fmac_f32_e32 v8, v87, v55
	v_fmac_f32_e32 v9, v88, v55
	v_cvt_f32_ubyte0_e32 v85, v34
	v_cvt_f32_ubyte1_e32 v86, v34
	v_cvt_f32_ubyte2_e32 v87, v34
	v_cvt_f32_ubyte3_e32 v88, v34
	v_fmac_f32_e32 v10, v85, v55
	v_fmac_f32_e32 v11, v86, v55
	v_fmac_f32_e32 v12, v87, v55
	v_fmac_f32_e32 v13, v88, v55
	v_cvt_f32_ubyte0_e32 v85, v35
	v_cvt_f32_ubyte1_e32 v86, v35
	v_cvt_f32_ubyte2_e32 v87, v35
	v_cvt_f32_ubyte3_e32 v88, v35
	v_fmac_f32_e32 v14, v85, v55
	v_fmac_f32_e32 v15, v86, v55
	v_fmac_f32_e32 v16, v87, v55
	v_fmac_f32_e32 v17, v88, v55
	s_waitcnt vmcnt(3)
	v_cvt_f32_ubyte0_e32 v85, v36
	v_cvt_f32_ubyte1_e32 v86, v36
	v_cvt_f32_ubyte2_e32 v87, v36
	v_cvt_f32_ubyte3_e32 v88, v36
	v_fmac_f32_e32 v2, v85, v56
	v_fmac_f32_e32 v3, v86, v56
	v_fmac_f32_e32 v4, v87, v56
	v_fmac_f32_e32 v5, v88, v56
	v_cvt_f32_ubyte0_e32 v85, v37
	v_cvt_f32_ubyte1_e32 v86, v37
	v_cvt_f32_ubyte2_e32 v87, v37
	v_cvt_f32_ubyte3_e32 v88, v37
	v_fmac_f32_e32 v6, v85, v56
	v_fmac_f32_e32 v7, v86, v56
	v_fmac_f32_e32 v8, v87, v56
	v_fmac_f32_e32 v9, v88, v56
	v_cvt_f32_ubyte0_e32 v85, v38
	v_cvt_f32_ubyte1_e32 v86, v38
	v_cvt_f32_ubyte2_e32 v87, v38
	v_cvt_f32_ubyte3_e32 v88, v38
	v_fmac_f32_e32 v10, v85, v56
	v_fmac_f32_e32 v11, v86, v56
	v_fmac_f32_e32 v12, v87, v56
	v_fmac_f32_e32 v13, v88, v56
	v_cvt_f32_ubyte0_e32 v85, v39
	v_cvt_f32_ubyte1_e32 v86, v39
	v_cvt_f32_ubyte2_e32 v87, v39
	v_cvt_f32_ubyte3_e32 v88, v39
	v_fmac_f32_e32 v14, v85, v56
	v_fmac_f32_e32 v15, v86, v56
	v_fmac_f32_e32 v16, v87, v56
	v_fmac_f32_e32 v17, v88, v56
	s_waitcnt vmcnt(2)
	v_cvt_f32_ubyte0_e32 v85, v40
	v_cvt_f32_ubyte1_e32 v86, v40
	v_cvt_f32_ubyte2_e32 v87, v40
	v_cvt_f32_ubyte3_e32 v88, v40
	v_fmac_f32_e32 v2, v85, v57
	v_fmac_f32_e32 v3, v86, v57
	v_fmac_f32_e32 v4, v87, v57
	v_fmac_f32_e32 v5, v88, v57
	v_cvt_f32_ubyte0_e32 v85, v41
	v_cvt_f32_ubyte1_e32 v86, v41
	v_cvt_f32_ubyte2_e32 v87, v41
	v_cvt_f32_ubyte3_e32 v88, v41
	v_fmac_f32_e32 v6, v85, v57
	v_fmac_f32_e32 v7, v86, v57
	v_fmac_f32_e32 v8, v87, v57
	v_fmac_f32_e32 v9, v88, v57
	v_cvt_f32_ubyte0_e32 v85, v42
	v_cvt_f32_ubyte1_e32 v86, v42
	v_cvt_f32_ubyte2_e32 v87, v42
	v_cvt_f32_ubyte3_e32 v88, v42
	v_fmac_f32_e32 v10, v85, v57
	v_fmac_f32_e32 v11, v86, v57
	v_fmac_f32_e32 v12, v87, v57
	v_fmac_f32_e32 v13, v88, v57
	v_cvt_f32_ubyte0_e32 v85, v43
	v_cvt_f32_ubyte1_e32 v86, v43
	v_cvt_f32_ubyte2_e32 v87, v43
	v_cvt_f32_ubyte3_e32 v88, v43
	v_fmac_f32_e32 v14, v85, v57
	v_fmac_f32_e32 v15, v86, v57
	v_fmac_f32_e32 v16, v87, v57
	v_fmac_f32_e32 v17, v88, v57
	s_waitcnt vmcnt(1)
	v_cvt_f32_ubyte0_e32 v85, v44
	v_cvt_f32_ubyte1_e32 v86, v44
	v_cvt_f32_ubyte2_e32 v87, v44
	v_cvt_f32_ubyte3_e32 v88, v44
	v_fmac_f32_e32 v2, v85, v58
	v_fmac_f32_e32 v3, v86, v58
	v_fmac_f32_e32 v4, v87, v58
	v_fmac_f32_e32 v5, v88, v58
	v_cvt_f32_ubyte0_e32 v85, v45
	v_cvt_f32_ubyte1_e32 v86, v45
	v_cvt_f32_ubyte2_e32 v87, v45
	v_cvt_f32_ubyte3_e32 v88, v45
	v_fmac_f32_e32 v6, v85, v58
	v_fmac_f32_e32 v7, v86, v58
	v_fmac_f32_e32 v8, v87, v58
	v_fmac_f32_e32 v9, v88, v58
	v_cvt_f32_ubyte0_e32 v85, v46
	v_cvt_f32_ubyte1_e32 v86, v46
	v_cvt_f32_ubyte2_e32 v87, v46
	v_cvt_f32_ubyte3_e32 v88, v46
	v_fmac_f32_e32 v10, v85, v58
	v_fmac_f32_e32 v11, v86, v58
	v_fmac_f32_e32 v12, v87, v58
	v_fmac_f32_e32 v13, v88, v58
	v_cvt_f32_ubyte0_e32 v85, v47
	v_cvt_f32_ubyte1_e32 v86, v47
	v_cvt_f32_ubyte2_e32 v87, v47
	v_cvt_f32_ubyte3_e32 v88, v47
	v_fmac_f32_e32 v14, v85, v58
	v_fmac_f32_e32 v15, v86, v58
	v_fmac_f32_e32 v16, v87, v58
	v_fmac_f32_e32 v17, v88, v58
	s_waitcnt vmcnt(0)
	v_cvt_f32_ubyte0_e32 v85, v48
	v_cvt_f32_ubyte1_e32 v86, v48
	v_cvt_f32_ubyte2_e32 v87, v48
	v_cvt_f32_ubyte3_e32 v88, v48
	v_fmac_f32_e32 v2, v85, v59
	v_fmac_f32_e32 v3, v86, v59
	v_fmac_f32_e32 v4, v87, v59
	v_fmac_f32_e32 v5, v88, v59
	v_cvt_f32_ubyte0_e32 v85, v49
	v_cvt_f32_ubyte1_e32 v86, v49
	v_cvt_f32_ubyte2_e32 v87, v49
	v_cvt_f32_ubyte3_e32 v88, v49
	v_fmac_f32_e32 v6, v85, v59
	v_fmac_f32_e32 v7, v86, v59
	v_fmac_f32_e32 v8, v87, v59
	v_fmac_f32_e32 v9, v88, v59
	v_cvt_f32_ubyte0_e32 v85, v50
	v_cvt_f32_ubyte1_e32 v86, v50
	v_cvt_f32_ubyte2_e32 v87, v50
	v_cvt_f32_ubyte3_e32 v88, v50
	v_fmac_f32_e32 v10, v85, v59
	v_fmac_f32_e32 v11, v86, v59
	v_fmac_f32_e32 v12, v87, v59
	v_fmac_f32_e32 v13, v88, v59
	v_cvt_f32_ubyte0_e32 v85, v51
	v_cvt_f32_ubyte1_e32 v86, v51
	v_cvt_f32_ubyte2_e32 v87, v51
	v_cvt_f32_ubyte3_e32 v88, v51
	v_fmac_f32_e32 v14, v85, v59
	v_fmac_f32_e32 v15, v86, v59
	v_fmac_f32_e32 v16, v87, v59
	v_fmac_f32_e32 v17, v88, v59
	s_branch .Lg2_rare_check
.Lg2_tailb0:
	s_waitcnt vmcnt(7)
	v_cvt_f32_ubyte0_e32 v85, v20
	v_cvt_f32_ubyte1_e32 v86, v20
	v_cvt_f32_ubyte2_e32 v87, v20
	v_cvt_f32_ubyte3_e32 v88, v20
	v_fmac_f32_e32 v2, v85, v52
	v_fmac_f32_e32 v3, v86, v52
	v_fmac_f32_e32 v4, v87, v52
	v_fmac_f32_e32 v5, v88, v52
	v_cvt_f32_ubyte0_e32 v85, v21
	v_cvt_f32_ubyte1_e32 v86, v21
	v_cvt_f32_ubyte2_e32 v87, v21
	v_cvt_f32_ubyte3_e32 v88, v21
	v_fmac_f32_e32 v6, v85, v52
	v_fmac_f32_e32 v7, v86, v52
	v_fmac_f32_e32 v8, v87, v52
	v_fmac_f32_e32 v9, v88, v52
	v_cvt_f32_ubyte0_e32 v85, v22
	v_cvt_f32_ubyte1_e32 v86, v22
	v_cvt_f32_ubyte2_e32 v87, v22
	v_cvt_f32_ubyte3_e32 v88, v22
	v_fmac_f32_e32 v10, v85, v52
	v_fmac_f32_e32 v11, v86, v52
	v_fmac_f32_e32 v12, v87, v52
	v_fmac_f32_e32 v13, v88, v52
	v_cvt_f32_ubyte0_e32 v85, v23
	v_cvt_f32_ubyte1_e32 v86, v23
	v_cvt_f32_ubyte2_e32 v87, v23
	v_cvt_f32_ubyte3_e32 v88, v23
	v_fmac_f32_e32 v14, v85, v52
	v_fmac_f32_e32 v15, v86, v52
	v_fmac_f32_e32 v16, v87, v52
	v_fmac_f32_e32 v17, v88, v52
	global_load_dwordx4 v[112:115], v103, s[10:11] offset:0
	s_waitcnt vmcnt(7)
	v_cvt_f32_ubyte0_e32 v85, v24
	v_cvt_f32_ubyte1_e32 v86, v24
	v_cvt_f32_ubyte2_e32 v87, v24
	v_cvt_f32_ubyte3_e32 v88, v24
	v_fmac_f32_e32 v2, v85, v53
	v_fmac_f32_e32 v3, v86, v53
	v_fmac_f32_e32 v4, v87, v53
	v_fmac_f32_e32 v5, v88, v53
	v_cvt_f32_ubyte0_e32 v85, v25
	v_cvt_f32_ubyte1_e32 v86, v25
	v_cvt_f32_ubyte2_e32 v87, v25
	v_cvt_f32_ubyte3_e32 v88, v25
	v_fmac_f32_e32 v6, v85, v53
	v_fmac_f32_e32 v7, v86, v53
	v_fmac_f32_e32 v8, v87, v53
	v_fmac_f32_e32 v9, v88, v53
	v_cvt_f32_ubyte0_e32 v85, v26
	v_cvt_f32_ubyte1_e32 v86, v26
	v_cvt_f32_ubyte2_e32 v87, v26
	v_cvt_f32_ubyte3_e32 v88, v26
	v_fmac_f32_e32 v10, v85, v53
	v_fmac_f32_e32 v11, v86, v53
	v_fmac_f32_e32 v12, v87, v53
	v_fmac_f32_e32 v13, v88, v53
	v_cvt_f32_ubyte0_e32 v85, v27
	v_cvt_f32_ubyte1_e32 v86, v27
	v_cvt_f32_ubyte2_e32 v87, v27
	v_cvt_f32_ubyte3_e32 v88, v27
	v_fmac_f32_e32 v14, v85, v53
	v_fmac_f32_e32 v15, v86, v53
	v_fmac_f32_e32 v16, v87, v53
	v_fmac_f32_e32 v17, v88, v53
	global_load_dwordx4 v[116:119], v103, s[10:11] offset:64
	s_waitcnt vmcnt(7)
	v_cvt_f32_ubyte0_e32 v85, v28
	v_cvt_f32_ubyte1_e32 v86, v28
	v_cvt_f32_ubyte2_e32 v87, v28
	v_cvt_f32_ubyte3_e32 v88, v28
	v_fmac_f32_e32 v2, v85, v54
	v_fmac_f32_e32 v3, v86, v54
	v_fmac_f32_e32 v4, v87, v54
	v_fmac_f32_e32 v5, v88, v54
	v_cvt_f32_ubyte0_e32 v85, v29
	v_cvt_f32_ubyte1_e32 v86, v29
	v_cvt_f32_ubyte2_e32 v87, v29
	v_cvt_f32_ubyte3_e32 v88, v29
	v_fmac_f32_e32 v6, v85, v54
	v_fmac_f32_e32 v7, v86, v54
	v_fmac_f32_e32 v8, v87, v54
	v_fmac_f32_e32 v9, v88, v54
	v_cvt_f32_ubyte0_e32 v85, v30
	v_cvt_f32_ubyte1_e32 v86, v30
	v_cvt_f32_ubyte2_e32 v87, v30
	v_cvt_f32_ubyte3_e32 v88, v30
	v_fmac_f32_e32 v10, v85, v54
	v_fmac_f32_e32 v11, v86, v54
	v_fmac_f32_e32 v12, v87, v54
	v_fmac_f32_e32 v13, v88, v54
	v_cvt_f32_ubyte0_e32 v85, v31
	v_cvt_f32_ubyte1_e32 v86, v31
	v_cvt_f32_ubyte2_e32 v87, v31
	v_cvt_f32_ubyte3_e32 v88, v31
	v_fmac_f32_e32 v14, v85, v54
	v_fmac_f32_e32 v15, v86, v54
	v_fmac_f32_e32 v16, v87, v54
	v_fmac_f32_e32 v17, v88, v54
	global_load_dwordx4 v[120:123], v103, s[10:11] offset:128
	s_waitcnt vmcnt(7)
	v_cvt_f32_ubyte0_e32 v85, v32
	v_cvt_f32_ubyte1_e32 v86, v32
	v_cvt_f32_ubyte2_e32 v87, v32
	v_cvt_f32_ubyte3_e32 v88, v32
	v_fmac_f32_e32 v2, v85, v55
	v_fmac_f32_e32 v3, v86, v55
	v_fmac_f32_e32 v4, v87, v55
	v_fmac_f32_e32 v5, v88, v55
	v_cvt_f32_ubyte0_e32 v85, v33
	v_cvt_f32_ubyte1_e32 v86, v33
	v_cvt_f32_ubyte2_e32 v87, v33
	v_cvt_f32_ubyte3_e32 v88, v33
	v_fmac_f32_e32 v6, v85, v55
	v_fmac_f32_e32 v7, v86, v55
	v_fmac_f32_e32 v8, v87, v55
	v_fmac_f32_e32 v9, v88, v55
	v_cvt_f32_ubyte0_e32 v85, v34
	v_cvt_f32_ubyte1_e32 v86, v34
	v_cvt_f32_ubyte2_e32 v87, v34
	v_cvt_f32_ubyte3_e32 v88, v34
	v_fmac_f32_e32 v10, v85, v55
	v_fmac_f32_e32 v11, v86, v55
	v_fmac_f32_e32 v12, v87, v55
	v_fmac_f32_e32 v13, v88, v55
	v_cvt_f32_ubyte0_e32 v85, v35
	v_cvt_f32_ubyte1_e32 v86, v35
	v_cvt_f32_ubyte2_e32 v87, v35
	v_cvt_f32_ubyte3_e32 v88, v35
	v_fmac_f32_e32 v14, v85, v55
	v_fmac_f32_e32 v15, v86, v55
	v_fmac_f32_e32 v16, v87, v55
	v_fmac_f32_e32 v17, v88, v55
	global_load_dwordx4 v[124:127], v103, s[10:11] offset:192
	s_waitcnt vmcnt(7)
	v_cvt_f32_ubyte0_e32 v85, v36
	v_cvt_f32_ubyte1_e32 v86, v36
	v_cvt_f32_ubyte2_e32 v87, v36
	v_cvt_f32_ubyte3_e32 v88, v36
	v_fmac_f32_e32 v2, v85, v56
	v_fmac_f32_e32 v3, v86, v56
	v_fmac_f32_e32 v4, v87, v56
	v_fmac_f32_e32 v5, v88, v56
	v_cvt_f32_ubyte0_e32 v85, v37
	v_cvt_f32_ubyte1_e32 v86, v37
	v_cvt_f32_ubyte2_e32 v87, v37
	v_cvt_f32_ubyte3_e32 v88, v37
	v_fmac_f32_e32 v6, v85, v56
	v_fmac_f32_e32 v7, v86, v56
	v_fmac_f32_e32 v8, v87, v56
	v_fmac_f32_e32 v9, v88, v56
	v_cvt_f32_ubyte0_e32 v85, v38
	v_cvt_f32_ubyte1_e32 v86, v38
	v_cvt_f32_ubyte2_e32 v87, v38
	v_cvt_f32_ubyte3_e32 v88, v38
	v_fmac_f32_e32 v10, v85, v56
	v_fmac_f32_e32 v11, v86, v56
	v_fmac_f32_e32 v12, v87, v56
	v_fmac_f32_e32 v13, v88, v56
	v_cvt_f32_ubyte0_e32 v85, v39
	v_cvt_f32_ubyte1_e32 v86, v39
	v_cvt_f32_ubyte2_e32 v87, v39
	v_cvt_f32_ubyte3_e32 v88, v39
	v_fmac_f32_e32 v14, v85, v56
	v_fmac_f32_e32 v15, v86, v56
	v_fmac_f32_e32 v16, v87, v56
	v_fmac_f32_e32 v17, v88, v56
	s_waitcnt vmcnt(6)
	v_cvt_f32_ubyte0_e32 v85, v40
	v_cvt_f32_ubyte1_e32 v86, v40
	v_cvt_f32_ubyte2_e32 v87, v40
	v_cvt_f32_ubyte3_e32 v88, v40
	v_fmac_f32_e32 v2, v85, v57
	v_fmac_f32_e32 v3, v86, v57
	v_fmac_f32_e32 v4, v87, v57
	v_fmac_f32_e32 v5, v88, v57
	v_cvt_f32_ubyte0_e32 v85, v41
	v_cvt_f32_ubyte1_e32 v86, v41
	v_cvt_f32_ubyte2_e32 v87, v41
	v_cvt_f32_ubyte3_e32 v88, v41
	v_fmac_f32_e32 v6, v85, v57
	v_fmac_f32_e32 v7, v86, v57
	v_fmac_f32_e32 v8, v87, v57
	v_fmac_f32_e32 v9, v88, v57
	v_cvt_f32_ubyte0_e32 v85, v42
	v_cvt_f32_ubyte1_e32 v86, v42
	v_cvt_f32_ubyte2_e32 v87, v42
	v_cvt_f32_ubyte3_e32 v88, v42
	v_fmac_f32_e32 v10, v85, v57
	v_fmac_f32_e32 v11, v86, v57
	v_fmac_f32_e32 v12, v87, v57
	v_fmac_f32_e32 v13, v88, v57
	v_cvt_f32_ubyte0_e32 v85, v43
	v_cvt_f32_ubyte1_e32 v86, v43
	v_cvt_f32_ubyte2_e32 v87, v43
	v_cvt_f32_ubyte3_e32 v88, v43
	v_fmac_f32_e32 v14, v85, v57
	v_fmac_f32_e32 v15, v86, v57
	v_fmac_f32_e32 v16, v87, v57
	v_fmac_f32_e32 v17, v88, v57
	s_waitcnt vmcnt(5)
	v_cvt_f32_ubyte0_e32 v85, v44
	v_cvt_f32_ubyte1_e32 v86, v44
	v_cvt_f32_ubyte2_e32 v87, v44
	v_cvt_f32_ubyte3_e32 v88, v44
	v_fmac_f32_e32 v2, v85, v58
	v_fmac_f32_e32 v3, v86, v58
	v_fmac_f32_e32 v4, v87, v58
	v_fmac_f32_e32 v5, v88, v58
	v_cvt_f32_ubyte0_e32 v85, v45
	v_cvt_f32_ubyte1_e32 v86, v45
	v_cvt_f32_ubyte2_e32 v87, v45
	v_cvt_f32_ubyte3_e32 v88, v45
	v_fmac_f32_e32 v6, v85, v58
	v_fmac_f32_e32 v7, v86, v58
	v_fmac_f32_e32 v8, v87, v58
	v_fmac_f32_e32 v9, v88, v58
	v_cvt_f32_ubyte0_e32 v85, v46
	v_cvt_f32_ubyte1_e32 v86, v46
	v_cvt_f32_ubyte2_e32 v87, v46
	v_cvt_f32_ubyte3_e32 v88, v46
	v_fmac_f32_e32 v10, v85, v58
	v_fmac_f32_e32 v11, v86, v58
	v_fmac_f32_e32 v12, v87, v58
	v_fmac_f32_e32 v13, v88, v58
	v_cvt_f32_ubyte0_e32 v85, v47
	v_cvt_f32_ubyte1_e32 v86, v47
	v_cvt_f32_ubyte2_e32 v87, v47
	v_cvt_f32_ubyte3_e32 v88, v47
	v_fmac_f32_e32 v14, v85, v58
	v_fmac_f32_e32 v15, v86, v58
	v_fmac_f32_e32 v16, v87, v58
	v_fmac_f32_e32 v17, v88, v58
	s_waitcnt vmcnt(4)
	v_cvt_f32_ubyte0_e32 v85, v48
	v_cvt_f32_ubyte1_e32 v86, v48
	v_cvt_f32_ubyte2_e32 v87, v48
	v_cvt_f32_ubyte3_e32 v88, v48
	v_fmac_f32_e32 v2, v85, v59
	v_fmac_f32_e32 v3, v86, v59
	v_fmac_f32_e32 v4, v87, v59
	v_fmac_f32_e32 v5, v88, v59
	v_cvt_f32_ubyte0_e32 v85, v49
	v_cvt_f32_ubyte1_e32 v86, v49
	v_cvt_f32_ubyte2_e32 v87, v49
	v_cvt_f32_ubyte3_e32 v88, v49
	v_fmac_f32_e32 v6, v85, v59
	v_fmac_f32_e32 v7, v86, v59
	v_fmac_f32_e32 v8, v87, v59
	v_fmac_f32_e32 v9, v88, v59
	v_cvt_f32_ubyte0_e32 v85, v50
	v_cvt_f32_ubyte1_e32 v86, v50
	v_cvt_f32_ubyte2_e32 v87, v50
	v_cvt_f32_ubyte3_e32 v88, v50
	v_fmac_f32_e32 v10, v85, v59
	v_fmac_f32_e32 v11, v86, v59
	v_fmac_f32_e32 v12, v87, v59
	v_fmac_f32_e32 v13, v88, v59
	v_cvt_f32_ubyte0_e32 v85, v51
	v_cvt_f32_ubyte1_e32 v86, v51
	v_cvt_f32_ubyte2_e32 v87, v51
	v_cvt_f32_ubyte3_e32 v88, v51
	v_fmac_f32_e32 v14, v85, v59
	v_fmac_f32_e32 v15, v86, v59
	v_fmac_f32_e32 v16, v87, v59
	v_fmac_f32_e32 v17, v88, v59
	s_branch .Lg2_rare_check
.Lg2_tail4:
	s_cmp_eq_u32 s39, 1
	s_cbranch_scc1 .Lg2_tailb4
	s_waitcnt vmcnt(7)
	v_cvt_f32_ubyte0_e32 v85, v36
	v_cvt_f32_ubyte1_e32 v86, v36
	v_cvt_f32_ubyte2_e32 v87, v36
	v_cvt_f32_ubyte3_e32 v88, v36
	v_fmac_f32_e32 v2, v85, v56
	v_fmac_f32_e32 v3, v86, v56
	v_fmac_f32_e32 v4, v87, v56
	v_fmac_f32_e32 v5, v88, v56
	v_cvt_f32_ubyte0_e32 v85, v37
	v_cvt_f32_ubyte1_e32 v86, v37
	v_cvt_f32_ubyte2_e32 v87, v37
	v_cvt_f32_ubyte3_e32 v88, v37
	v_fmac_f32_e32 v6, v85, v56
	v_fmac_f32_e32 v7, v86, v56
	v_fmac_f32_e32 v8, v87, v56
	v_fmac_f32_e32 v9, v88, v56
	v_cvt_f32_ubyte0_e32 v85, v38
	v_cvt_f32_ubyte1_e32 v86, v38
	v_cvt_f32_ubyte2_e32 v87, v38
	v_cvt_f32_ubyte3_e32 v88, v38
	v_fmac_f32_e32 v10, v85, v56
	v_fmac_f32_e32 v11, v86, v56
	v_fmac_f32_e32 v12, v87, v56
	v_fmac_f32_e32 v13, v88, v56
	v_cvt_f32_ubyte0_e32 v85, v39
	v_cvt_f32_ubyte1_e32 v86, v39
	v_cvt_f32_ubyte2_e32 v87, v39
	v_cvt_f32_ubyte3_e32 v88, v39
	v_fmac_f32_e32 v14, v85, v56
	v_fmac_f32_e32 v15, v86, v56
	v_fmac_f32_e32 v16, v87, v56
	v_fmac_f32_e32 v17, v88, v56
	s_waitcnt vmcnt(6)
	v_cvt_f32_ubyte0_e32 v85, v40
	v_cvt_f32_ubyte1_e32 v86, v40
	v_cvt_f32_ubyte2_e32 v87, v40
	v_cvt_f32_ubyte3_e32 v88, v40
	v_fmac_f32_e32 v2, v85, v57
	v_fmac_f32_e32 v3, v86, v57
	v_fmac_f32_e32 v4, v87, v57
	v_fmac_f32_e32 v5, v88, v57
	v_cvt_f32_ubyte0_e32 v85, v41
	v_cvt_f32_ubyte1_e32 v86, v41
	v_cvt_f32_ubyte2_e32 v87, v41
	v_cvt_f32_ubyte3_e32 v88, v41
	v_fmac_f32_e32 v6, v85, v57
	v_fmac_f32_e32 v7, v86, v57
	v_fmac_f32_e32 v8, v87, v57
	v_fmac_f32_e32 v9, v88, v57
	v_cvt_f32_ubyte0_e32 v85, v42
	v_cvt_f32_ubyte1_e32 v86, v42
	v_cvt_f32_ubyte2_e32 v87, v42
	v_cvt_f32_ubyte3_e32 v88, v42
	v_fmac_f32_e32 v10, v85, v57
	v_fmac_f32_e32 v11, v86, v57
	v_fmac_f32_e32 v12, v87, v57
	v_fmac_f32_e32 v13, v88, v57
	v_cvt_f32_ubyte0_e32 v85, v43
	v_cvt_f32_ubyte1_e32 v86, v43
	v_cvt_f32_ubyte2_e32 v87, v43
	v_cvt_f32_ubyte3_e32 v88, v43
	v_fmac_f32_e32 v14, v85, v57
	v_fmac_f32_e32 v15, v86, v57
	v_fmac_f32_e32 v16, v87, v57
	v_fmac_f32_e32 v17, v88, v57
	s_waitcnt vmcnt(5)
	v_cvt_f32_ubyte0_e32 v85, v44
	v_cvt_f32_ubyte1_e32 v86, v44
	v_cvt_f32_ubyte2_e32 v87, v44
	v_cvt_f32_ubyte3_e32 v88, v44
	v_fmac_f32_e32 v2, v85, v58
	v_fmac_f32_e32 v3, v86, v58
	v_fmac_f32_e32 v4, v87, v58
	v_fmac_f32_e32 v5, v88, v58
	v_cvt_f32_ubyte0_e32 v85, v45
	v_cvt_f32_ubyte1_e32 v86, v45
	v_cvt_f32_ubyte2_e32 v87, v45
	v_cvt_f32_ubyte3_e32 v88, v45
	v_fmac_f32_e32 v6, v85, v58
	v_fmac_f32_e32 v7, v86, v58
	v_fmac_f32_e32 v8, v87, v58
	v_fmac_f32_e32 v9, v88, v58
	v_cvt_f32_ubyte0_e32 v85, v46
	v_cvt_f32_ubyte1_e32 v86, v46
	v_cvt_f32_ubyte2_e32 v87, v46
	v_cvt_f32_ubyte3_e32 v88, v46
	v_fmac_f32_e32 v10, v85, v58
	v_fmac_f32_e32 v11, v86, v58
	v_fmac_f32_e32 v12, v87, v58
	v_fmac_f32_e32 v13, v88, v58
	v_cvt_f32_ubyte0_e32 v85, v47
	v_cvt_f32_ubyte1_e32 v86, v47
	v_cvt_f32_ubyte2_e32 v87, v47
	v_cvt_f32_ubyte3_e32 v88, v47
	v_fmac_f32_e32 v14, v85, v58
	v_fmac_f32_e32 v15, v86, v58
	v_fmac_f32_e32 v16, v87, v58
	v_fmac_f32_e32 v17, v88, v58
	s_waitcnt vmcnt(4)
	v_cvt_f32_ubyte0_e32 v85, v48
	v_cvt_f32_ubyte1_e32 v86, v48
	v_cvt_f32_ubyte2_e32 v87, v48
	v_cvt_f32_ubyte3_e32 v88, v48
	v_fmac_f32_e32 v2, v85, v59
	v_fmac_f32_e32 v3, v86, v59
	v_fmac_f32_e32 v4, v87, v59
	v_fmac_f32_e32 v5, v88, v59
	v_cvt_f32_ubyte0_e32 v85, v49
	v_cvt_f32_ubyte1_e32 v86, v49
	v_cvt_f32_ubyte2_e32 v87, v49
	v_cvt_f32_ubyte3_e32 v88, v49
	v_fmac_f32_e32 v6, v85, v59
	v_fmac_f32_e32 v7, v86, v59
	v_fmac_f32_e32 v8, v87, v59
	v_fmac_f32_e32 v9, v88, v59
	v_cvt_f32_ubyte0_e32 v85, v50
	v_cvt_f32_ubyte1_e32 v86, v50
	v_cvt_f32_ubyte2_e32 v87, v50
	v_cvt_f32_ubyte3_e32 v88, v50
	v_fmac_f32_e32 v10, v85, v59
	v_fmac_f32_e32 v11, v86, v59
	v_fmac_f32_e32 v12, v87, v59
	v_fmac_f32_e32 v13, v88, v59
	v_cvt_f32_ubyte0_e32 v85, v51
	v_cvt_f32_ubyte1_e32 v86, v51
	v_cvt_f32_ubyte2_e32 v87, v51
	v_cvt_f32_ubyte3_e32 v88, v51
	v_fmac_f32_e32 v14, v85, v59
	v_fmac_f32_e32 v15, v86, v59
	v_fmac_f32_e32 v16, v87, v59
	v_fmac_f32_e32 v17, v88, v59
	s_waitcnt vmcnt(3)
	v_cvt_f32_ubyte0_e32 v85, v20
	v_cvt_f32_ubyte1_e32 v86, v20
	v_cvt_f32_ubyte2_e32 v87, v20
	v_cvt_f32_ubyte3_e32 v88, v20
	v_fmac_f32_e32 v2, v85, v52
	v_fmac_f32_e32 v3, v86, v52
	v_fmac_f32_e32 v4, v87, v52
	v_fmac_f32_e32 v5, v88, v52
	v_cvt_f32_ubyte0_e32 v85, v21
	v_cvt_f32_ubyte1_e32 v86, v21
	v_cvt_f32_ubyte2_e32 v87, v21
	v_cvt_f32_ubyte3_e32 v88, v21
	v_fmac_f32_e32 v6, v85, v52
	v_fmac_f32_e32 v7, v86, v52
	v_fmac_f32_e32 v8, v87, v52
	v_fmac_f32_e32 v9, v88, v52
	v_cvt_f32_ubyte0_e32 v85, v22
	v_cvt_f32_ubyte1_e32 v86, v22
	v_cvt_f32_ubyte2_e32 v87, v22
	v_cvt_f32_ubyte3_e32 v88, v22
	v_fmac_f32_e32 v10, v85, v52
	v_fmac_f32_e32 v11, v86, v52
	v_fmac_f32_e32 v12, v87, v52
	v_fmac_f32_e32 v13, v88, v52
	v_cvt_f32_ubyte0_e32 v85, v23
	v_cvt_f32_ubyte1_e32 v86, v23
	v_cvt_f32_ubyte2_e32 v87, v23
	v_cvt_f32_ubyte3_e32 v88, v23
	v_fmac_f32_e32 v14, v85, v52
	v_fmac_f32_e32 v15, v86, v52
	v_fmac_f32_e32 v16, v87, v52
	v_fmac_f32_e32 v17, v88, v52
	s_waitcnt vmcnt(2)
	v_cvt_f32_ubyte0_e32 v85, v24
	v_cvt_f32_ubyte1_e32 v86, v24
	v_cvt_f32_ubyte2_e32 v87, v24
	v_cvt_f32_ubyte3_e32 v88, v24
	v_fmac_f32_e32 v2, v85, v53
	v_fmac_f32_e32 v3, v86, v53
	v_fmac_f32_e32 v4, v87, v53
	v_fmac_f32_e32 v5, v88, v53
	v_cvt_f32_ubyte0_e32 v85, v25
	v_cvt_f32_ubyte1_e32 v86, v25
	v_cvt_f32_ubyte2_e32 v87, v25
	v_cvt_f32_ubyte3_e32 v88, v25
	v_fmac_f32_e32 v6, v85, v53
	v_fmac_f32_e32 v7, v86, v53
	v_fmac_f32_e32 v8, v87, v53
	v_fmac_f32_e32 v9, v88, v53
	v_cvt_f32_ubyte0_e32 v85, v26
	v_cvt_f32_ubyte1_e32 v86, v26
	v_cvt_f32_ubyte2_e32 v87, v26
	v_cvt_f32_ubyte3_e32 v88, v26
	v_fmac_f32_e32 v10, v85, v53
	v_fmac_f32_e32 v11, v86, v53
	v_fmac_f32_e32 v12, v87, v53
	v_fmac_f32_e32 v13, v88, v53
	v_cvt_f32_ubyte0_e32 v85, v27
	v_cvt_f32_ubyte1_e32 v86, v27
	v_cvt_f32_ubyte2_e32 v87, v27
	v_cvt_f32_ubyte3_e32 v88, v27
	v_fmac_f32_e32 v14, v85, v53
	v_fmac_f32_e32 v15, v86, v53
	v_fmac_f32_e32 v16, v87, v53
	v_fmac_f32_e32 v17, v88, v53
	s_waitcnt vmcnt(1)
	v_cvt_f32_ubyte0_e32 v85, v28
	v_cvt_f32_ubyte1_e32 v86, v28
	v_cvt_f32_ubyte2_e32 v87, v28
	v_cvt_f32_ubyte3_e32 v88, v28
	v_fmac_f32_e32 v2, v85, v54
	v_fmac_f32_e32 v3, v86, v54
	v_fmac_f32_e32 v4, v87, v54
	v_fmac_f32_e32 v5, v88, v54
	v_cvt_f32_ubyte0_e32 v85, v29
	v_cvt_f32_ubyte1_e32 v86, v29
	v_cvt_f32_ubyte2_e32 v87, v29
	v_cvt_f32_ubyte3_e32 v88, v29
	v_fmac_f32_e32 v6, v85, v54
	v_fmac_f32_e32 v7, v86, v54
	v_fmac_f32_e32 v8, v87, v54
	v_fmac_f32_e32 v9, v88, v54
	v_cvt_f32_ubyte0_e32 v85, v30
	v_cvt_f32_ubyte1_e32 v86, v30
	v_cvt_f32_ubyte2_e32 v87, v30
	v_cvt_f32_ubyte3_e32 v88, v30
	v_fmac_f32_e32 v10, v85, v54
	v_fmac_f32_e32 v11, v86, v54
	v_fmac_f32_e32 v12, v87, v54
	v_fmac_f32_e32 v13, v88, v54
	v_cvt_f32_ubyte0_e32 v85, v31
	v_cvt_f32_ubyte1_e32 v86, v31
	v_cvt_f32_ubyte2_e32 v87, v31
	v_cvt_f32_ubyte3_e32 v88, v31
	v_fmac_f32_e32 v14, v85, v54
	v_fmac_f32_e32 v15, v86, v54
	v_fmac_f32_e32 v16, v87, v54
	v_fmac_f32_e32 v17, v88, v54
	s_waitcnt vmcnt(0)
	v_cvt_f32_ubyte0_e32 v85, v32
	v_cvt_f32_ubyte1_e32 v86, v32
	v_cvt_f32_ubyte2_e32 v87, v32
	v_cvt_f32_ubyte3_e32 v88, v32
	v_fmac_f32_e32 v2, v85, v55
	v_fmac_f32_e32 v3, v86, v55
	v_fmac_f32_e32 v4, v87, v55
	v_fmac_f32_e32 v5, v88, v55
	v_cvt_f32_ubyte0_e32 v85, v33
	v_cvt_f32_ubyte1_e32 v86, v33
	v_cvt_f32_ubyte2_e32 v87, v33
	v_cvt_f32_ubyte3_e32 v88, v33
	v_fmac_f32_e32 v6, v85, v55
	v_fmac_f32_e32 v7, v86, v55
	v_fmac_f32_e32 v8, v87, v55
	v_fmac_f32_e32 v9, v88, v55
	v_cvt_f32_ubyte0_e32 v85, v34
	v_cvt_f32_ubyte1_e32 v86, v34
	v_cvt_f32_ubyte2_e32 v87, v34
	v_cvt_f32_ubyte3_e32 v88, v34
	v_fmac_f32_e32 v10, v85, v55
	v_fmac_f32_e32 v11, v86, v55
	v_fmac_f32_e32 v12, v87, v55
	v_fmac_f32_e32 v13, v88, v55
	v_cvt_f32_ubyte0_e32 v85, v35
	v_cvt_f32_ubyte1_e32 v86, v35
	v_cvt_f32_ubyte2_e32 v87, v35
	v_cvt_f32_ubyte3_e32 v88, v35
	v_fmac_f32_e32 v14, v85, v55
	v_fmac_f32_e32 v15, v86, v55
	v_fmac_f32_e32 v16, v87, v55
	v_fmac_f32_e32 v17, v88, v55
	s_branch .Lg2_rare_check
.Lg2_tailb4:
	s_waitcnt vmcnt(7)
	v_cvt_f32_ubyte0_e32 v85, v36
	v_cvt_f32_ubyte1_e32 v86, v36
	v_cvt_f32_ubyte2_e32 v87, v36
	v_cvt_f32_ubyte3_e32 v88, v36
	v_fmac_f32_e32 v2, v85, v56
	v_fmac_f32_e32 v3, v86, v56
	v_fmac_f32_e32 v4, v87, v56
	v_fmac_f32_e32 v5, v88, v56
	v_cvt_f32_ubyte0_e32 v85, v37
	v_cvt_f32_ubyte1_e32 v86, v37
	v_cvt_f32_ubyte2_e32 v87, v37
	v_cvt_f32_ubyte3_e32 v88, v37
	v_fmac_f32_e32 v6, v85, v56
	v_fmac_f32_e32 v7, v86, v56
	v_fmac_f32_e32 v8, v87, v56
	v_fmac_f32_e32 v9, v88, v56
	v_cvt_f32_ubyte0_e32 v85, v38
	v_cvt_f32_ubyte1_e32 v86, v38
	v_cvt_f32_ubyte2_e32 v87, v38
	v_cvt_f32_ubyte3_e32 v88, v38
	v_fmac_f32_e32 v10, v85, v56
	v_fmac_f32_e32 v11, v86, v56
	v_fmac_f32_e32 v12, v87, v56
	v_fmac_f32_e32 v13, v88, v56
	v_cvt_f32_ubyte0_e32 v85, v39
	v_cvt_f32_ubyte1_e32 v86, v39
	v_cvt_f32_ubyte2_e32 v87, v39
	v_cvt_f32_ubyte3_e32 v88, v39
	v_fmac_f32_e32 v14, v85, v56
	v_fmac_f32_e32 v15, v86, v56
	v_fmac_f32_e32 v16, v87, v56
	v_fmac_f32_e32 v17, v88, v56
	global_load_dwordx4 v[112:115], v103, s[10:11] offset:0
	s_waitcnt vmcnt(7)
	v_cvt_f32_ubyte0_e32 v85, v40
	v_cvt_f32_ubyte1_e32 v86, v40
	v_cvt_f32_ubyte2_e32 v87, v40
	v_cvt_f32_ubyte3_e32 v88, v40
	v_fmac_f32_e32 v2, v85, v57
	v_fmac_f32_e32 v3, v86, v57
	v_fmac_f32_e32 v4, v87, v57
	v_fmac_f32_e32 v5, v88, v57
	v_cvt_f32_ubyte0_e32 v85, v41
	v_cvt_f32_ubyte1_e32 v86, v41
	v_cvt_f32_ubyte2_e32 v87, v41
	v_cvt_f32_ubyte3_e32 v88, v41
	v_fmac_f32_e32 v6, v85, v57
	v_fmac_f32_e32 v7, v86, v57
	v_fmac_f32_e32 v8, v87, v57
	v_fmac_f32_e32 v9, v88, v57
	v_cvt_f32_ubyte0_e32 v85, v42
	v_cvt_f32_ubyte1_e32 v86, v42
	v_cvt_f32_ubyte2_e32 v87, v42
	v_cvt_f32_ubyte3_e32 v88, v42
	v_fmac_f32_e32 v10, v85, v57
	v_fmac_f32_e32 v11, v86, v57
	v_fmac_f32_e32 v12, v87, v57
	v_fmac_f32_e32 v13, v88, v57
	v_cvt_f32_ubyte0_e32 v85, v43
	v_cvt_f32_ubyte1_e32 v86, v43
	v_cvt_f32_ubyte2_e32 v87, v43
	v_cvt_f32_ubyte3_e32 v88, v43
	v_fmac_f32_e32 v14, v85, v57
	v_fmac_f32_e32 v15, v86, v57
	v_fmac_f32_e32 v16, v87, v57
	v_fmac_f32_e32 v17, v88, v57
	global_load_dwordx4 v[116:119], v103, s[10:11] offset:64
	s_waitcnt vmcnt(7)
	v_cvt_f32_ubyte0_e32 v85, v44
	v_cvt_f32_ubyte1_e32 v86, v44
	v_cvt_f32_ubyte2_e32 v87, v44
	v_cvt_f32_ubyte3_e32 v88, v44
	v_fmac_f32_e32 v2, v85, v58
	v_fmac_f32_e32 v3, v86, v58
	v_fmac_f32_e32 v4, v87, v58
	v_fmac_f32_e32 v5, v88, v58
	v_cvt_f32_ubyte0_e32 v85, v45
	v_cvt_f32_ubyte1_e32 v86, v45
	v_cvt_f32_ubyte2_e32 v87, v45
	v_cvt_f32_ubyte3_e32 v88, v45
	v_fmac_f32_e32 v6, v85, v58
	v_fmac_f32_e32 v7, v86, v58
	v_fmac_f32_e32 v8, v87, v58
	v_fmac_f32_e32 v9, v88, v58
	v_cvt_f32_ubyte0_e32 v85, v46
	v_cvt_f32_ubyte1_e32 v86, v46
	v_cvt_f32_ubyte2_e32 v87, v46
	v_cvt_f32_ubyte3_e32 v88, v46
	v_fmac_f32_e32 v10, v85, v58
	v_fmac_f32_e32 v11, v86, v58
	v_fmac_f32_e32 v12, v87, v58
	v_fmac_f32_e32 v13, v88, v58
	v_cvt_f32_ubyte0_e32 v85, v47
	v_cvt_f32_ubyte1_e32 v86, v47
	v_cvt_f32_ubyte2_e32 v87, v47
	v_cvt_f32_ubyte3_e32 v88, v47
	v_fmac_f32_e32 v14, v85, v58
	v_fmac_f32_e32 v15, v86, v58
	v_fmac_f32_e32 v16, v87, v58
	v_fmac_f32_e32 v17, v88, v58
	global_load_dwordx4 v[120:123], v103, s[10:11] offset:128
	s_waitcnt vmcnt(7)
	v_cvt_f32_ubyte0_e32 v85, v48
	v_cvt_f32_ubyte1_e32 v86, v48
	v_cvt_f32_ubyte2_e32 v87, v48
	v_cvt_f32_ubyte3_e32 v88, v48
	v_fmac_f32_e32 v2, v85, v59
	v_fmac_f32_e32 v3, v86, v59
	v_fmac_f32_e32 v4, v87, v59
	v_fmac_f32_e32 v5, v88, v59
	v_cvt_f32_ubyte0_e32 v85, v49
	v_cvt_f32_ubyte1_e32 v86, v49
	v_cvt_f32_ubyte2_e32 v87, v49
	v_cvt_f32_ubyte3_e32 v88, v49
	v_fmac_f32_e32 v6, v85, v59
	v_fmac_f32_e32 v7, v86, v59
	v_fmac_f32_e32 v8, v87, v59
	v_fmac_f32_e32 v9, v88, v59
	v_cvt_f32_ubyte0_e32 v85, v50
	v_cvt_f32_ubyte1_e32 v86, v50
	v_cvt_f32_ubyte2_e32 v87, v50
	v_cvt_f32_ubyte3_e32 v88, v50
	v_fmac_f32_e32 v10, v85, v59
	v_fmac_f32_e32 v11, v86, v59
	v_fmac_f32_e32 v12, v87, v59
	v_fmac_f32_e32 v13, v88, v59
	v_cvt_f32_ubyte0_e32 v85, v51
	v_cvt_f32_ubyte1_e32 v86, v51
	v_cvt_f32_ubyte2_e32 v87, v51
	v_cvt_f32_ubyte3_e32 v88, v51
	v_fmac_f32_e32 v14, v85, v59
	v_fmac_f32_e32 v15, v86, v59
	v_fmac_f32_e32 v16, v87, v59
	v_fmac_f32_e32 v17, v88, v59
	global_load_dwordx4 v[124:127], v103, s[10:11] offset:192
	s_waitcnt vmcnt(7)
	v_cvt_f32_ubyte0_e32 v85, v20
	v_cvt_f32_ubyte1_e32 v86, v20
	v_cvt_f32_ubyte2_e32 v87, v20
	v_cvt_f32_ubyte3_e32 v88, v20
	v_fmac_f32_e32 v2, v85, v52
	v_fmac_f32_e32 v3, v86, v52
	v_fmac_f32_e32 v4, v87, v52
	v_fmac_f32_e32 v5, v88, v52
	v_cvt_f32_ubyte0_e32 v85, v21
	v_cvt_f32_ubyte1_e32 v86, v21
	v_cvt_f32_ubyte2_e32 v87, v21
	v_cvt_f32_ubyte3_e32 v88, v21
	v_fmac_f32_e32 v6, v85, v52
	v_fmac_f32_e32 v7, v86, v52
	v_fmac_f32_e32 v8, v87, v52
	v_fmac_f32_e32 v9, v88, v52
	v_cvt_f32_ubyte0_e32 v85, v22
	v_cvt_f32_ubyte1_e32 v86, v22
	v_cvt_f32_ubyte2_e32 v87, v22
	v_cvt_f32_ubyte3_e32 v88, v22
	v_fmac_f32_e32 v10, v85, v52
	v_fmac_f32_e32 v11, v86, v52
	v_fmac_f32_e32 v12, v87, v52
	v_fmac_f32_e32 v13, v88, v52
	v_cvt_f32_ubyte0_e32 v85, v23
	v_cvt_f32_ubyte1_e32 v86, v23
	v_cvt_f32_ubyte2_e32 v87, v23
	v_cvt_f32_ubyte3_e32 v88, v23
	v_fmac_f32_e32 v14, v85, v52
	v_fmac_f32_e32 v15, v86, v52
	v_fmac_f32_e32 v16, v87, v52
	v_fmac_f32_e32 v17, v88, v52
	s_waitcnt vmcnt(6)
	v_cvt_f32_ubyte0_e32 v85, v24
	v_cvt_f32_ubyte1_e32 v86, v24
	v_cvt_f32_ubyte2_e32 v87, v24
	v_cvt_f32_ubyte3_e32 v88, v24
	v_fmac_f32_e32 v2, v85, v53
	v_fmac_f32_e32 v3, v86, v53
	v_fmac_f32_e32 v4, v87, v53
	v_fmac_f32_e32 v5, v88, v53
	v_cvt_f32_ubyte0_e32 v85, v25
	v_cvt_f32_ubyte1_e32 v86, v25
	v_cvt_f32_ubyte2_e32 v87, v25
	v_cvt_f32_ubyte3_e32 v88, v25
	v_fmac_f32_e32 v6, v85, v53
	v_fmac_f32_e32 v7, v86, v53
	v_fmac_f32_e32 v8, v87, v53
	v_fmac_f32_e32 v9, v88, v53
	v_cvt_f32_ubyte0_e32 v85, v26
	v_cvt_f32_ubyte1_e32 v86, v26
	v_cvt_f32_ubyte2_e32 v87, v26
	v_cvt_f32_ubyte3_e32 v88, v26
	v_fmac_f32_e32 v10, v85, v53
	v_fmac_f32_e32 v11, v86, v53
	v_fmac_f32_e32 v12, v87, v53
	v_fmac_f32_e32 v13, v88, v53
	v_cvt_f32_ubyte0_e32 v85, v27
	v_cvt_f32_ubyte1_e32 v86, v27
	v_cvt_f32_ubyte2_e32 v87, v27
	v_cvt_f32_ubyte3_e32 v88, v27
	v_fmac_f32_e32 v14, v85, v53
	v_fmac_f32_e32 v15, v86, v53
	v_fmac_f32_e32 v16, v87, v53
	v_fmac_f32_e32 v17, v88, v53
	s_waitcnt vmcnt(5)
	v_cvt_f32_ubyte0_e32 v85, v28
	v_cvt_f32_ubyte1_e32 v86, v28
	v_cvt_f32_ubyte2_e32 v87, v28
	v_cvt_f32_ubyte3_e32 v88, v28
	v_fmac_f32_e32 v2, v85, v54
	v_fmac_f32_e32 v3, v86, v54
	v_fmac_f32_e32 v4, v87, v54
	v_fmac_f32_e32 v5, v88, v54
	v_cvt_f32_ubyte0_e32 v85, v29
	v_cvt_f32_ubyte1_e32 v86, v29
	v_cvt_f32_ubyte2_e32 v87, v29
	v_cvt_f32_ubyte3_e32 v88, v29
	v_fmac_f32_e32 v6, v85, v54
	v_fmac_f32_e32 v7, v86, v54
	v_fmac_f32_e32 v8, v87, v54
	v_fmac_f32_e32 v9, v88, v54
	v_cvt_f32_ubyte0_e32 v85, v30
	v_cvt_f32_ubyte1_e32 v86, v30
	v_cvt_f32_ubyte2_e32 v87, v30
	v_cvt_f32_ubyte3_e32 v88, v30
	v_fmac_f32_e32 v10, v85, v54
	v_fmac_f32_e32 v11, v86, v54
	v_fmac_f32_e32 v12, v87, v54
	v_fmac_f32_e32 v13, v88, v54
	v_cvt_f32_ubyte0_e32 v85, v31
	v_cvt_f32_ubyte1_e32 v86, v31
	v_cvt_f32_ubyte2_e32 v87, v31
	v_cvt_f32_ubyte3_e32 v88, v31
	v_fmac_f32_e32 v14, v85, v54
	v_fmac_f32_e32 v15, v86, v54
	v_fmac_f32_e32 v16, v87, v54
	v_fmac_f32_e32 v17, v88, v54
	s_waitcnt vmcnt(4)
	v_cvt_f32_ubyte0_e32 v85, v32
	v_cvt_f32_ubyte1_e32 v86, v32
	v_cvt_f32_ubyte2_e32 v87, v32
	v_cvt_f32_ubyte3_e32 v88, v32
	v_fmac_f32_e32 v2, v85, v55
	v_fmac_f32_e32 v3, v86, v55
	v_fmac_f32_e32 v4, v87, v55
	v_fmac_f32_e32 v5, v88, v55
	v_cvt_f32_ubyte0_e32 v85, v33
	v_cvt_f32_ubyte1_e32 v86, v33
	v_cvt_f32_ubyte2_e32 v87, v33
	v_cvt_f32_ubyte3_e32 v88, v33
	v_fmac_f32_e32 v6, v85, v55
	v_fmac_f32_e32 v7, v86, v55
	v_fmac_f32_e32 v8, v87, v55
	v_fmac_f32_e32 v9, v88, v55
	v_cvt_f32_ubyte0_e32 v85, v34
	v_cvt_f32_ubyte1_e32 v86, v34
	v_cvt_f32_ubyte2_e32 v87, v34
	v_cvt_f32_ubyte3_e32 v88, v34
	v_fmac_f32_e32 v10, v85, v55
	v_fmac_f32_e32 v11, v86, v55
	v_fmac_f32_e32 v12, v87, v55
	v_fmac_f32_e32 v13, v88, v55
	v_cvt_f32_ubyte0_e32 v85, v35
	v_cvt_f32_ubyte1_e32 v86, v35
	v_cvt_f32_ubyte2_e32 v87, v35
	v_cvt_f32_ubyte3_e32 v88, v35
	v_fmac_f32_e32 v14, v85, v55
	v_fmac_f32_e32 v15, v86, v55
	v_fmac_f32_e32 v16, v87, v55
	v_fmac_f32_e32 v17, v88, v55
	s_branch .Lg2_rare_check
